# MoE phases: skip the overflow-item id scan when no expert exceeds a main item's row capacity (per-wave check of the 256 counts)
# speedup vs baseline: 1.0007x; 1.0007x over previous
.LBB0_1279:
	s_cmp_le_i32 s74, s2
	s_cselect_b64 s[2:3], -1, 0
	s_and_b64 s[0:1], s[2:3], s[0:1]
	v_writelane_b32 v255, s0, 11
	s_andn2_b64 vcc, exec, s[0:1]
	s_nop 0
	v_writelane_b32 v255, s1, 12
	s_cbranch_vccnz .LBB0_1346
	v_readlane_b32 s0, v254, 41
	v_readlane_b32 s2, v254, 60
	v_readlane_b32 s3, v254, 61
	v_mov_b32_e32 v0, s0
	s_waitcnt vmcnt(0)
	ds_read_b64 v[2:3], v0
	s_mov_b32 s3, s57
	s_lshl_b32 s56, s2, 13
	s_lshl_b32 s0, s2, 8
	v_writelane_b32 v254, s2, 60
	s_waitcnt lgkmcnt(0)
	v_readfirstlane_b32 s15, v2
	s_lshl_b64 s[8:9], s[56:57], 2
	v_writelane_b32 v254, s3, 61
	s_lshl_b64 s[2:3], s[2:3], 28
	v_readfirstlane_b32 s16, v3
	s_add_u32 s8, s15, s8
	v_readlane_b32 s11, v253, 0
	s_addc_u32 s9, s16, s9
	v_mbcnt_lo_u32_b32 v0, -1, 0
	v_mbcnt_hi_u32_b32 v0, -1, v0
	s_mov_b32 s1, s57
	v_add_u32_e32 v231, s11, v0
	s_add_u32 s50, s8, 0x10000
	v_readfirstlane_b32 s8, v231
	s_addc_u32 s51, s9, 0
	s_ashr_i32 s9, s8, 6
	s_lshl_b64 s[18:19], s[0:1], 2
	s_add_u32 s0, s15, s18
	v_writelane_b32 v255, s18, 13
	s_addc_u32 s1, s16, s19
	s_add_u32 s52, s0, 0xa000
	s_addc_u32 s53, s1, 0
	v_readlane_b32 s11, v254, 53
	v_writelane_b32 v255, s19, 14
	s_add_u32 s0, s15, 0x2e3e0000
	v_mov_b32_e32 v0, s11
	v_writelane_b32 v255, s0, 15
	s_addc_u32 s0, s16, 0
	ds_read_b128 v[2:5], v0
	s_add_u32 s54, s15, 0x4ffe0a00
	s_addc_u32 s55, s16, 0
	s_add_u32 s58, s15, 0x2f3e0000
	v_writelane_b32 v255, s0, 16
	s_addc_u32 s59, s16, 0
	s_ashr_i32 s0, s8, 7
	s_and_b32 s1, s9, 1
	v_writelane_b32 v255, s15, 17
	s_lshl_b32 s28, s0, 5
	s_lshl_b32 s15, s1, 5
	s_waitcnt lgkmcnt(0)
	v_readfirstlane_b32 s11, v2
	v_readfirstlane_b32 s13, v4
	s_cmp_lt_i32 s0, 2
	v_readfirstlane_b32 s12, v3
	v_readfirstlane_b32 s14, v5
	s_cselect_b32 s11, s11, s13
	s_cselect_b32 s0, s12, s14
	s_add_u32 s2, s11, s2
	v_writelane_b32 v255, s16, 18
	s_addc_u32 s0, s0, s3
	s_lshl_b32 s3, s9, 8
	v_writelane_b32 v255, s15, 5
	s_add_i32 s3, s3, 0
	v_writelane_b32 v255, s3, 7
	s_and_b32 s3, s8, 0x80
	s_add_u32 s2, s2, s3
	s_addc_u32 s0, s0, 0
	s_and_b32 s83, s8, 0xffffffc0
	v_writelane_b32 v255, s2, 19
	s_lshl_b32 s2, s83, 2
	s_add_i32 s87, s2, 0
	s_ashr_i32 s2, s8, 8
	v_writelane_b32 v255, s0, 20
	s_lshl_b32 s0, s9, 5
	s_lshl_b32 s3, s2, 13
	s_and_b32 s0, s0, 0xffffff80
	s_add_i32 s3, s3, 0
	s_lshl_b32 s1, s1, 12
	s_add_i32 s0, s0, 0
	s_add_i32 s78, s3, s1
	v_writelane_b32 v255, s0, 9
	s_and_b32 s0, s9, 3
	s_or_b32 s80, s83, 32
	s_add_i32 s78, s78, 0x10000
	s_cmp_gt_u32 s0, 1
	s_cselect_b64 s[60:61], -1, 0
	s_cmp_lt_u32 s0, 2
	s_mul_i32 s33, s0, 0x1200
	s_cselect_b64 s[62:63], -1, 0
	s_lshl_b32 s64, s0, 5
	s_lshl_b32 s0, s9, 4
	s_and_b32 s0, s0, 16
	v_cmp_eq_u32_e64 s[18:19], 0, v231
	v_writelane_b32 v255, s0, 3
	s_lshl_b32 s1, s2, 7
	v_writelane_b32 v255, s18, 21
	s_add_i32 s3, s1, 0
	s_mov_b32 s65, s57
	v_writelane_b32 v255, s19, 22
	v_mbcnt_lo_u32_b32 v0, -1, 0
	v_mbcnt_hi_u32_b32 v0, -1, v0
	v_lshlrev_b32_e32 v0, 7, v0
	v_add_u32_e32 v2, 0x2000, v0
	v_add_u32_e32 v3, 0x4000, v0
	v_add_u32_e32 v4, 0x6000, v0
	global_load_dword v5, v0, s[50:51]
	global_load_dword v2, v2, s[50:51]
	global_load_dword v3, v3, s[50:51]
	global_load_dword v4, v4, s[50:51]
	s_movk_i32 s100, 0x240
	s_waitcnt vmcnt(0)
	v_max3_i32 v2, v2, v3, v4
	v_max_i32_e32 v2, v2, v5
	v_cmp_lt_i32_e32 vcc, s100, v2
	s_nop 1
	s_cmp_lg_u64 vcc, 0
	s_cselect_b64 s[100:101], -1, 0
	s_branch .LBB0_1283

.LBB0_1288:
	s_or_b64 exec, exec, s[12:13]
	s_waitcnt vmcnt(0)
	v_readfirstlane_b32 s2, v2
	s_mov_b64 s[14:15], -1
	s_nop 0
	v_add_u32_e32 v2, s2, v0
	v_cmp_lt_u32_e32 vcc, 0xff, v2
	s_andn2_b64 vcc, vcc, s[100:101]
	v_mov_b32_e32 v5, 0x500
	s_nop 0
	v_cndmask_b32_e32 v2, v2, v5, vcc
	v_add_u32_e32 v0, 0xffffff00, v2
	s_movk_i32 s2, 0x400
	v_cmp_gt_u32_e32 vcc, s2, v0
	s_and_saveexec_b64 s[12:13], vcc
	s_cbranch_execz .LBB0_1285
	v_lshlrev_b32_e32 v0, 5, v2
	v_and_b32_e32 v0, 0xff80, v0
	v_lshl_add_u64 v[4:5], s[50:51], 0, v[0:1]
	v_add_co_u32_e32 v4, vcc, 0xffffe000, v4
	s_movk_i32 s2, 0x240
	s_nop 0
	v_addc_co_u32_e32 v5, vcc, -1, v5, vcc
	global_load_dword v0, v[4:5], off
	s_waitcnt vmcnt(0)
	v_cmp_lt_i32_e32 vcc, s2, v0
	s_orn2_b64 s[14:15], vcc, exec
	s_branch .LBB0_1285

.LBB0_1402:
	s_cmp_le_i32 s74, s2
	s_cselect_b64 s[2:3], -1, 0
	s_and_b64 s[8:9], s[2:3], s[0:1]
	s_andn2_b64 vcc, exec, s[8:9]
	s_cbranch_vccnz .LBB0_1456
	v_readlane_b32 s2, v254, 60
	v_readlane_b32 s0, v254, 41
	v_readlane_b32 s3, v254, 61
	s_mov_b32 s3, s57
	v_mov_b32_e32 v0, s0
	s_waitcnt vmcnt(0)
	ds_read_b64 v[2:3], v0
	s_lshl_b32 s56, s2, 13
	s_lshl_b64 s[12:13], s[2:3], 28
	v_writelane_b32 v254, s2, 60
	v_readlane_b32 s11, v253, 0
	v_mbcnt_lo_u32_b32 v0, -1, 0
	v_mbcnt_hi_u32_b32 v0, -1, v0
	s_lshl_b32 s0, s2, 8
	v_writelane_b32 v254, s3, 61
	v_add_u32_e32 v231, s11, v0
	v_readlane_b32 s11, v254, 55
	s_waitcnt lgkmcnt(0)
	v_readfirstlane_b32 s2, v2
	v_readfirstlane_b32 s3, v3
	v_mov_b32_e32 v0, s11
	ds_read_b64 v[2:3], v0
	s_or_b32 s14, s0, 64
	s_lshl_b64 s[0:1], s[56:57], 2
	s_add_u32 s0, s2, s0
	s_addc_u32 s1, s3, s1
	s_add_u32 s0, s0, 0x10000
	v_readfirstlane_b32 s33, v231
	s_addc_u32 s1, s1, 0
	s_ashr_i32 s25, s33, 6
	s_waitcnt lgkmcnt(0)
	v_readfirstlane_b32 s11, v2
	s_mov_b32 s15, s57
	v_readfirstlane_b32 s16, v3
	s_add_u32 s27, s11, s12
	s_addc_u32 s34, s16, s13
	s_lshl_b64 s[14:15], s[14:15], 2
	s_add_u32 s11, s2, s14
	s_addc_u32 s12, s3, s15
	s_add_u32 s16, s11, 0xa000
	s_addc_u32 s17, s12, 0
	s_add_u32 s11, s2, 0x2e3e0000
	s_addc_u32 s26, s3, 0
	s_add_u32 s18, s2, 0x2e360000
	s_addc_u32 s19, s3, 0
	s_add_u32 s30, s2, 0x2f3e0000
	s_addc_u32 s31, s3, 0
	s_add_u32 s12, s2, 0x33be0200
	s_addc_u32 s13, s3, 0
	s_lshl_b32 s28, s25, 4
	v_bfe_u32 v3, v231, 3, 3
	v_and_b32_e32 v2, 7, v231
	v_and_or_b32 v3, s28, 16, v3
	s_andn2_b32 s28, s28, 31
	v_lshlrev_b32_e32 v4, 4, v2
	v_or_b32_e32 v2, s28, v2
	s_movk_i32 s35, 0x90
	s_ashr_i32 s29, s28, 31
	v_mul_lo_u32 v2, v2, s35
	s_lshl_b32 s35, s25, 8
	s_add_i32 s35, s35, 0
	s_lshl_b64 s[28:29], s[28:29], 2
	s_add_u32 s27, s27, s28
	s_addc_u32 s28, s34, s29
	s_lshl_b32 s34, s25, 5
	v_and_b32_e32 v0, 31, v231
	s_and_b32 s29, s34, 0xffffff80
	v_and_b32_e32 v232, 32, v231
	v_lshl_add_u32 v234, v3, 2, v2
	v_mul_u32_u24_e32 v2, 0x48, v0
	v_lshlrev_b32_e32 v0, 2, v0
	s_add_i32 s29, s29, 0
	s_andn2_b32 s33, s33, 63
	s_and_b32 s38, s25, 3
	v_cmp_eq_u32_e64 s[40:41], 0, v231
	v_lshl_or_b32 v233, v3, 13, v4
	v_add_lshl_u32 v235, v2, v232, 1
	v_add_u32_e32 v236, s35, v0
	v_add_u32_e32 v237, s29, v0
	s_mulk_i32 s38, 0x1200
	s_or_b32 s39, s33, 32
	s_and_b32 s34, s34, 0x60
	s_mov_b32 s35, s57
	v_mbcnt_lo_u32_b32 v0, -1, 0
	v_mbcnt_hi_u32_b32 v0, -1, v0
	v_lshlrev_b32_e32 v0, 7, v0
	v_add_u32_e32 v2, 0x2000, v0
	v_add_u32_e32 v3, 0x4000, v0
	v_add_u32_e32 v4, 0x6000, v0
	global_load_dword v5, v0, s[0:1]
	global_load_dword v2, v2, s[0:1]
	global_load_dword v3, v3, s[0:1]
	global_load_dword v4, v4, s[0:1]
	s_movk_i32 s100, 0x240
	s_waitcnt vmcnt(0)
	v_max3_i32 v2, v2, v3, v4
	v_max_i32_e32 v2, v2, v5
	v_cmp_lt_i32_e32 vcc, s100, v2
	s_nop 1
	s_cmp_lg_u64 vcc, 0
	s_cselect_b64 s[100:101], -1, 0
	s_branch .LBB0_1406

.LBB0_1411:
	s_or_b64 exec, exec, s[44:45]
	s_waitcnt vmcnt(0)
	v_readfirstlane_b32 s25, v2
	s_mov_b64 s[46:47], -1
	s_nop 0
	v_add_u32_e32 v2, s25, v0
	v_cmp_lt_u32_e32 vcc, 0xff, v2
	s_andn2_b64 vcc, vcc, s[100:101]
	v_mov_b32_e32 v5, 0x500
	s_nop 0
	v_cndmask_b32_e32 v2, v2, v5, vcc
	v_add_u32_e32 v0, 0xffffff00, v2
	s_movk_i32 s25, 0x400
	v_cmp_gt_u32_e32 vcc, s25, v0
	s_and_saveexec_b64 s[44:45], vcc
	s_cbranch_execz .LBB0_1408
	v_lshlrev_b32_e32 v0, 5, v2
	v_and_b32_e32 v0, 0xff80, v0
	v_lshl_add_u64 v[4:5], s[0:1], 0, v[0:1]
	v_add_co_u32_e32 v4, vcc, 0xffffe000, v4
	s_movk_i32 s25, 0x240
	s_nop 0
	v_addc_co_u32_e32 v5, vcc, -1, v5, vcc
	global_load_dword v0, v[4:5], off
	s_waitcnt vmcnt(0)
	v_cmp_lt_i32_e32 vcc, s25, v0
	s_orn2_b64 s[46:47], vcc, exec
	s_branch .LBB0_1408

	.amdhsa_kernel _Z3fwd4Args
		.amdhsa_group_segment_fixed_size 0
		.amdhsa_private_segment_fixed_size 0
		.amdhsa_kernarg_size 408
		.amdhsa_user_sgpr_count 2
		.amdhsa_user_sgpr_dispatch_ptr 0
		.amdhsa_user_sgpr_queue_ptr 0
		.amdhsa_user_sgpr_kernarg_segment_ptr 1
		.amdhsa_user_sgpr_dispatch_id 0
		.amdhsa_user_sgpr_kernarg_preload_length 0
		.amdhsa_user_sgpr_kernarg_preload_offset 0
		.amdhsa_user_sgpr_private_segment_size 0
		.amdhsa_uses_dynamic_stack 0
		.amdhsa_enable_private_segment 0
		.amdhsa_system_sgpr_workgroup_id_x 1
		.amdhsa_system_sgpr_workgroup_id_y 0
		.amdhsa_system_sgpr_workgroup_id_z 0
		.amdhsa_system_sgpr_workgroup_info 0
		.amdhsa_system_vgpr_workitem_id 0
		.amdhsa_next_free_vgpr 256
		.amdhsa_next_free_sgpr 102
		.amdhsa_accum_offset 256
		.amdhsa_reserve_vcc 1
		.amdhsa_float_round_mode_32 0
		.amdhsa_float_round_mode_16_64 0
		.amdhsa_float_denorm_mode_32 3
		.amdhsa_float_denorm_mode_16_64 3
		.amdhsa_dx10_clamp 1
		.amdhsa_ieee_mode 1
		.amdhsa_fp16_overflow 0
		.amdhsa_tg_split 0
		.amdhsa_exception_fp_ieee_invalid_op 0
		.amdhsa_exception_fp_denorm_src 0
		.amdhsa_exception_fp_ieee_div_zero 0
		.amdhsa_exception_fp_ieee_overflow 0
		.amdhsa_exception_fp_ieee_underflow 0
		.amdhsa_exception_fp_ieee_inexact 0
		.amdhsa_exception_int_div_zero 0
	.end_amdhsa_kernel

amdhsa.kernels:
  - .agpr_count:     0
    .args:
      - .offset:         0
        .size:           152
        .value_kind:     by_value
      - .offset:         152
        .size:           4
        .value_kind:     hidden_block_count_x
      - .offset:         156
        .size:           4
        .value_kind:     hidden_block_count_y
      - .offset:         160
        .size:           4
        .value_kind:     hidden_block_count_z
      - .offset:         164
        .size:           2
        .value_kind:     hidden_group_size_x
      - .offset:         166
        .size:           2
        .value_kind:     hidden_group_size_y
      - .offset:         168
        .size:           2
        .value_kind:     hidden_group_size_z
      - .offset:         170
        .size:           2
        .value_kind:     hidden_remainder_x
      - .offset:         172
        .size:           2
        .value_kind:     hidden_remainder_y
      - .offset:         174
        .size:           2
        .value_kind:     hidden_remainder_z
      - .offset:         192
        .size:           8
        .value_kind:     hidden_global_offset_x
      - .offset:         200
        .size:           8
        .value_kind:     hidden_global_offset_y
      - .offset:         208
        .size:           8
        .value_kind:     hidden_global_offset_z
      - .offset:         216
        .size:           2
        .value_kind:     hidden_grid_dims
      - .offset:         272
        .size:           4
        .value_kind:     hidden_dynamic_lds_size
    .group_segment_fixed_size: 0
    .kernarg_segment_align: 8
    .kernarg_segment_size: 408
    .language:       OpenCL C
    .language_version:
      - 2
      - 0
    .max_flat_workgroup_size: 512
    .name:           _Z3fwd4Args
    .private_segment_fixed_size: 0
    .sgpr_count:     108
    .sgpr_spill_count: 161
    .symbol:         _Z3fwd4Args.kd
    .uniform_work_group_size: 1
    .uses_dynamic_stack: false
    .vgpr_count:     256
    .vgpr_spill_count: 0
    .wavefront_size: 64
